# speedup vs baseline: 1.0027x; 1.0027x over previous
amdhsa.kernels:
  - .agpr_count:     0
    .args:
      - .actual_access:  read_only
        .address_space:  global
        .offset:         0
        .size:           8
        .value_kind:     global_buffer
      - .actual_access:  read_only
        .address_space:  global
        .offset:         8
        .size:           8
        .value_kind:     global_buffer
      - .actual_access:  write_only
        .address_space:  global
        .offset:         16
        .size:           8
        .value_kind:     global_buffer
      - .actual_access:  write_only
        .address_space:  global
        .offset:         24
        .size:           8
        .value_kind:     global_buffer
      - .actual_access:  read_only
        .address_space:  global
        .offset:         32
        .size:           8
        .value_kind:     global_buffer
      - .actual_access:  read_only
        .address_space:  global
        .offset:         40
        .size:           8
        .value_kind:     global_buffer
      - .actual_access:  read_only
        .address_space:  global
        .offset:         48
        .size:           8
        .value_kind:     global_buffer
      - .actual_access:  read_only
        .address_space:  global
        .offset:         56
        .size:           8
        .value_kind:     global_buffer
      - .actual_access:  read_only
        .address_space:  global
        .offset:         64
        .size:           8
        .value_kind:     global_buffer
      - .actual_access:  write_only
        .address_space:  global
        .offset:         72
        .size:           8
        .value_kind:     global_buffer
      - .actual_access:  write_only
        .address_space:  global
        .offset:         80
        .size:           8
        .value_kind:     global_buffer
      - .actual_access:  write_only
        .address_space:  global
        .offset:         88
        .size:           8
        .value_kind:     global_buffer
      - .actual_access:  write_only
        .address_space:  global
        .offset:         96
        .size:           8
        .value_kind:     global_buffer
      - .actual_access:  write_only
        .address_space:  global
        .offset:         104
        .size:           8
        .value_kind:     global_buffer
      - .actual_access:  write_only
        .address_space:  global
        .offset:         112
        .size:           8
        .value_kind:     global_buffer
      - .offset:         120
        .size:           4
        .value_kind:     hidden_block_count_x
      - .offset:         124
        .size:           4
        .value_kind:     hidden_block_count_y
      - .offset:         128
        .size:           4
        .value_kind:     hidden_block_count_z
      - .offset:         132
        .size:           2
        .value_kind:     hidden_group_size_x
      - .offset:         134
        .size:           2
        .value_kind:     hidden_group_size_y
      - .offset:         136
        .size:           2
        .value_kind:     hidden_group_size_z
      - .offset:         138
        .size:           2
        .value_kind:     hidden_remainder_x
      - .offset:         140
        .size:           2
        .value_kind:     hidden_remainder_y
      - .offset:         142
        .size:           2
        .value_kind:     hidden_remainder_z
      - .offset:         160
        .size:           8
        .value_kind:     hidden_global_offset_x
      - .offset:         168
        .size:           8
        .value_kind:     hidden_global_offset_y
      - .offset:         176
        .size:           8
        .value_kind:     hidden_global_offset_z
      - .offset:         184
        .size:           2
        .value_kind:     hidden_grid_dims
    .group_segment_fixed_size: 21520
    .kernarg_segment_align: 8
    .kernarg_segment_size: 376
    .language:       OpenCL C
    .language_version:
      - 2
      - 0
    .max_flat_workgroup_size: 1024
    .name:           _Z11k_chunksortPKiS0_PjS1_PKfS3_S3_S3_S3_PDF16_S4_PfS5_S4_Ph
    .private_segment_fixed_size: 0
    .sgpr_count:     32
    .sgpr_spill_count: 0
    .symbol:         _Z11k_chunksortPKiS0_PjS1_PKfS3_S3_S3_S3_PDF16_S4_PfS5_S4_Ph.kd
    .uniform_work_group_size: 1
    .uses_dynamic_stack: false
    .vgpr_count:     38
    .vgpr_spill_count: 0
    .wavefront_size: 64
  - .agpr_count:     0
    .args:
      - .actual_access:  read_only
        .address_space:  global
        .offset:         0
        .size:           8
        .value_kind:     global_buffer
      - .actual_access:  read_only
        .address_space:  global
        .offset:         8
        .size:           8
        .value_kind:     global_buffer
      - .actual_access:  read_only
        .address_space:  global
        .offset:         16
        .size:           8
        .value_kind:     global_buffer
      - .actual_access:  write_only
        .address_space:  global
        .offset:         24
        .size:           8
        .value_kind:     global_buffer
      - .actual_access:  write_only
        .address_space:  global
        .offset:         32
        .size:           8
        .value_kind:     global_buffer
      - .actual_access:  write_only
        .address_space:  global
        .offset:         40
        .size:           8
        .value_kind:     global_buffer
      - .actual_access:  write_only
        .address_space:  global
        .offset:         48
        .size:           8
        .value_kind:     global_buffer
    .group_segment_fixed_size: 22536
    .kernarg_segment_align: 8
    .kernarg_segment_size: 56
    .language:       OpenCL C
    .language_version:
      - 2
      - 0
    .max_flat_workgroup_size: 1024
    .name:           _Z5k_csrPKjS0_PKfPjPfPDF16_P15HIP_vector_typeIjLj4EE
    .private_segment_fixed_size: 0
    .sgpr_count:     54
    .sgpr_spill_count: 0
    .symbol:         _Z5k_csrPKjS0_PKfPjPfPDF16_P15HIP_vector_typeIjLj4EE.kd
    .uniform_work_group_size: 1
    .uses_dynamic_stack: false
    .vgpr_count:     56
    .vgpr_spill_count: 0
    .wavefront_size: 64
  - .agpr_count:     0
    .args:
      - .actual_access:  read_only
        .address_space:  global
        .offset:         0
        .size:           8
        .value_kind:     global_buffer
      - .actual_access:  read_only
        .address_space:  global
        .offset:         8
        .size:           8
        .value_kind:     global_buffer
      - .actual_access:  read_only
        .address_space:  global
        .offset:         16
        .size:           8
        .value_kind:     global_buffer
      - .actual_access:  read_only
        .address_space:  global
        .offset:         24
        .size:           8
        .value_kind:     global_buffer
      - .actual_access:  read_only
        .address_space:  global
        .offset:         32
        .size:           8
        .value_kind:     global_buffer
      - .actual_access:  read_only
        .address_space:  global
        .offset:         40
        .size:           8
        .value_kind:     global_buffer
      - .actual_access:  read_only
        .address_space:  global
        .offset:         48
        .size:           8
        .value_kind:     global_buffer
      - .actual_access:  write_only
        .address_space:  global
        .offset:         56
        .size:           8
        .value_kind:     global_buffer
      - .actual_access:  write_only
        .address_space:  global
        .offset:         64
        .size:           8
        .value_kind:     global_buffer
    .group_segment_fixed_size: 36112
    .kernarg_segment_align: 8
    .kernarg_segment_size: 72
    .language:       OpenCL C
    .language_version:
      - 2
      - 0
    .max_flat_workgroup_size: 256
    .name:           _Z8k_layer1PKfPKDF16_PK15HIP_vector_typeIjLj4EEPKjS0_S2_S0_PhPf
    .private_segment_fixed_size: 0
    .sgpr_count:     30
    .sgpr_spill_count: 0
    .symbol:         _Z8k_layer1PKfPKDF16_PK15HIP_vector_typeIjLj4EEPKjS0_S2_S0_PhPf.kd
    .uniform_work_group_size: 1
    .uses_dynamic_stack: false
    .vgpr_count:     128
    .vgpr_spill_count: 0
    .wavefront_size: 64
  - .agpr_count:     0
    .args:
      - .actual_access:  read_only
        .address_space:  global
        .offset:         0
        .size:           8
        .value_kind:     global_buffer
      - .actual_access:  read_only
        .address_space:  global
        .offset:         8
        .size:           8
        .value_kind:     global_buffer
      - .actual_access:  read_only
        .address_space:  global
        .offset:         16
        .size:           8
        .value_kind:     global_buffer
      - .actual_access:  read_only
        .address_space:  global
        .offset:         24
        .size:           8
        .value_kind:     global_buffer
      - .actual_access:  read_only
        .address_space:  global
        .offset:         32
        .size:           8
        .value_kind:     global_buffer
      - .actual_access:  read_only
        .address_space:  global
        .offset:         40
        .size:           8
        .value_kind:     global_buffer
      - .actual_access:  read_only
        .address_space:  global
        .offset:         48
        .size:           8
        .value_kind:     global_buffer
      - .address_space:  global
        .offset:         56
        .size:           8
        .value_kind:     global_buffer
    .group_segment_fixed_size: 39168
    .kernarg_segment_align: 8
    .kernarg_segment_size: 64
    .language:       OpenCL C
    .language_version:
      - 2
      - 0
    .max_flat_workgroup_size: 256
    .name:           _Z8k_layer2PKhPKfPK15HIP_vector_typeIjLj4EEPKjS2_PKDF16_S2_Pf
    .private_segment_fixed_size: 0
    .sgpr_count:     27
    .sgpr_spill_count: 0
    .symbol:         _Z8k_layer2PKhPKfPK15HIP_vector_typeIjLj4EEPKjS2_PKDF16_S2_Pf.kd
    .uniform_work_group_size: 1
    .uses_dynamic_stack: false
    .vgpr_count:     112
    .vgpr_spill_count: 0
    .wavefront_size: 64
  - .agpr_count:     0
    .args:
      - .actual_access:  read_only
        .address_space:  global
        .offset:         0
        .size:           8
        .value_kind:     global_buffer
      - .actual_access:  read_only
        .address_space:  global
        .offset:         8
        .size:           8
        .value_kind:     global_buffer
      - .actual_access:  read_only
        .address_space:  global
        .offset:         16
        .size:           8
        .value_kind:     global_buffer
      - .actual_access:  read_only
        .address_space:  global
        .offset:         24
        .size:           8
        .value_kind:     global_buffer
      - .actual_access:  read_only
        .address_space:  global
        .offset:         32
        .size:           8
        .value_kind:     global_buffer
      - .actual_access:  write_only
        .address_space:  global
        .offset:         40
        .size:           8
        .value_kind:     global_buffer
    .group_segment_fixed_size: 512
    .kernarg_segment_align: 8
    .kernarg_segment_size: 48
    .language:       OpenCL C
    .language_version:
      - 2
      - 0
    .max_flat_workgroup_size: 320
    .name:           _Z7k_headsPKfS0_S0_S0_S0_Pf
    .private_segment_fixed_size: 0
    .sgpr_count:     22
    .sgpr_spill_count: 0
    .symbol:         _Z7k_headsPKfS0_S0_S0_S0_Pf.kd
    .uniform_work_group_size: 1
    .uses_dynamic_stack: false
    .vgpr_count:     56
    .vgpr_spill_count: 0
    .wavefront_size: 64
